# MoE unit scheduler without LDS round trips (prefix table cached in a VGPR, readlane + ballot)
# baseline (speedup 1.0000x reference)
.LBB0_1847:
	s_or_b64 exec, exec, s[0:1]
	v_readlane_b32 s0, v254, 4
	s_mov_b32 s2, 0
	s_mov_b32 s4, s0
	v_readlane_b32 s54, v254, 2
	v_readlane_b32 s0, v254, 3
	s_waitcnt lgkmcnt(0)
	s_barrier
	v_readlane_b32 s100, v254, 26
	v_and_b32_e32 v251, 63, v0
	s_nop 1
	v_lshl_add_u32 v251, v251, 2, s100
	ds_read_b32 v251, v251
	s_mov_b32 s0, 23
	s_ashr_i32 s1, s0, 31
	s_lshl_b64 s[0:1], s[0:1], 3
	s_add_u32 s0, s94, s0
	s_addc_u32 s1, s95, s1
	s_load_dwordx2 s[24:25], s[0:1], 0x0
	v_readlane_b32 s0, v254, 50
	v_mov_b32_e32 v5, v0
	s_ashr_i32 s5, s4, 31
	v_mov_b32_e32 v2, s0
	ds_read_b32 v2, v2
	s_mov_b32 s55, 0
	v_readfirstlane_b32 s26, v5
	s_mov_b32 s3, 8
	s_mov_b64 s[0:1], s[4:5]
	s_waitcnt lgkmcnt(0)
	v_readfirstlane_b32 s6, v2
	s_ashr_i32 s7, s6, 31
	s_lshl_b64 s[10:11], s[6:7], 3
	v_mov_b64_e32 v[6:7], s[10:11]
	v_cmp_ge_i64_e32 vcc, s[4:5], v[6:7]
	v_cmp_lt_i64_e64 s[8:9], s[4:5], v[6:7]
	s_cbranch_vccz .LBB0_1849
	s_sub_u32 s0, s4, s10
	s_subb_u32 s1, s5, s11
	s_lshl_b64 s[6:7], s[6:7], 2
	v_mov_b64_e32 v[6:7], s[6:7]
	v_cmp_lt_i64_e64 s[8:9], s[0:1], v[6:7]
	s_mov_b32 s3, 4
	s_mov_b32 s55, 1

.LBB0_1891:
	s_add_i32 s87, s86, 1
	s_mul_hi_i32 s1, s87, s54
	s_mul_i32 s0, s87, s54
	s_add_u32 s0, s0, s4
	s_addc_u32 s1, s1, s5
	s_mov_b32 s2, 8
	s_waitcnt lgkmcnt(0)
	v_readlane_b32 s36, v251, 32
	s_ashr_i32 s37, s36, 31
	s_lshl_b64 s[40:41], s[36:37], 3
	v_mov_b64_e32 v[4:5], s[40:41]
	v_cmp_lt_i64_e64 s[38:39], s[0:1], v[4:5]
	s_and_b64 vcc, exec, s[38:39]
	s_mov_b32 s3, 0
	s_cbranch_vccnz .LBB0_1893
	s_sub_u32 s0, s0, s40
	s_subb_u32 s1, s1, s41
	s_lshl_b64 s[2:3], s[36:37], 2
	v_mov_b64_e32 v[4:5], s[2:3]
	v_cmp_lt_i64_e64 s[38:39], s[0:1], v[4:5]
	s_mov_b32 s2, 4
	s_mov_b32 s3, 1

.LBB0_1897:
	s_mov_b64 s[42:43], -1
	s_mov_b32 s88, s3
	v_cmp_ge_i32_e64 s[100:101], s28, v251
	s_nop 3
	s_and_b32 s100, s100, 0xfffffffe
	s_bcnt1_i32_b32 s1, s100
	v_readlane_b32 s29, v251, s1
	s_lshl_b32 s30, s1, 6
	s_sub_i32 s29, s28, s29
	s_add_i32 s30, s29, s30
	s_mul_i32 s29, s28, s2
	s_sub_i32 s29, s0, s29
	s_mul_i32 s0, s1, s2
	s_add_i32 s34, s0, s29
